# baseline (speedup 1.0000x reference)
.Lc7_l4:
	s_or_b64 exec, exec, s[6:7]
	s_and_saveexec_b64 s[38:39], s[40:41]
	s_cbranch_execz .Ln0b_skip
	s_lshl_b32 s62, s63, 6
	s_add_u32 s30, s30, s62
	s_addc_u32 s31, s31, 0
	s_add_u32 s32, s32, s62
	s_addc_u32 s33, s33, 0
	s_lshl_b32 s62, s63, 9
	s_add_u32 s34, s34, s62
	s_addc_u32 s35, s35, 0
	s_lshl_b32 s62, s63, 5
	v_lshlrev_b32_e32 v60, 7, v59
	v_add_u32_e32 v60, s62, v60
	v_and_b32_e32 v62, 3, v58
	v_xor_b32_e32 v62, s63, v62
	v_lshlrev_b32_e32 v62, 5, v62
	v_lshl_add_u32 v61, v58, 7, v62
	v_add_u32_e32 v61, 0x1740, v61
	v_mov_b32_e32 v44, 0
	v_mov_b32_e32 v45, 0
	v_mov_b32_e32 v46, 0
	v_mov_b32_e32 v47, 0
	v_mov_b32_e32 v48, 0
	v_mov_b32_e32 v49, 0
	v_mov_b32_e32 v50, 0
	v_mov_b32_e32 v51, 0
	s_load_dwordx2 s[40:41], s[30:31], 0x0
	s_load_dwordx2 s[42:43], s[30:31], 0x100
	s_load_dwordx2 s[44:45], s[30:31], 0x200
	s_load_dwordx2 s[46:47], s[30:31], 0x300
	s_load_dwordx2 s[48:49], s[30:31], 0x400
	s_load_dwordx2 s[50:51], s[30:31], 0x500
	s_load_dwordx2 s[52:53], s[30:31], 0x600
	s_load_dwordx2 s[54:55], s[30:31], 0x700
	s_load_dwordx2 s[56:57], s[30:31], 0x800
	s_load_dwordx2 s[58:59], s[30:31], 0x900
	s_load_dwordx2 s[60:61], s[32:33], 0x0
	s_load_dwordx16 s[64:79], s[34:35], 0x0
	s_waitcnt lgkmcnt(0)
	v_mov_b32_e32 v42, s60
	v_mov_b32_e32 v43, s61
	v_pk_fma_f32 v[42:43], v[32:33], s[40:41], v[42:43] op_sel_hi:[0,1,1]
	v_pk_fma_f32 v[42:43], v[32:33], s[42:43], v[42:43] op_sel:[1,0,0]
	v_pk_fma_f32 v[42:43], v[34:35], s[44:45], v[42:43] op_sel_hi:[0,1,1]
	v_pk_fma_f32 v[42:43], v[34:35], s[46:47], v[42:43] op_sel:[1,0,0]
	v_pk_fma_f32 v[42:43], v[36:37], s[48:49], v[42:43] op_sel_hi:[0,1,1]
	v_pk_fma_f32 v[42:43], v[36:37], s[50:51], v[42:43] op_sel:[1,0,0]
	v_pk_fma_f32 v[42:43], v[38:39], s[52:53], v[42:43] op_sel_hi:[0,1,1]
	v_pk_fma_f32 v[42:43], v[38:39], s[54:55], v[42:43] op_sel:[1,0,0]
	v_pk_fma_f32 v[42:43], v[40:41], s[56:57], v[42:43] op_sel_hi:[0,1,1]
	v_pk_fma_f32 v[42:43], v[40:41], s[58:59], v[42:43] op_sel:[1,0,0]
	v_max_f32_e32 v42, 0, v42
	v_max_f32_e32 v43, 0, v43
	v_cvt_pk_f16_f32 v52, v42, v43
	v_pk_fma_f32 v[44:45], v[42:43], s[64:65], v[44:45] op_sel_hi:[0,1,1]
	v_pk_fma_f32 v[46:47], v[42:43], s[66:67], v[46:47] op_sel_hi:[0,1,1]
	v_pk_fma_f32 v[48:49], v[42:43], s[68:69], v[48:49] op_sel_hi:[0,1,1]
	v_pk_fma_f32 v[50:51], v[42:43], s[70:71], v[50:51] op_sel_hi:[0,1,1]
	v_pk_fma_f32 v[44:45], v[42:43], s[72:73], v[44:45] op_sel:[1,0,0]
	v_pk_fma_f32 v[46:47], v[42:43], s[74:75], v[46:47] op_sel:[1,0,0]
	v_pk_fma_f32 v[48:49], v[42:43], s[76:77], v[48:49] op_sel:[1,0,0]
	v_pk_fma_f32 v[50:51], v[42:43], s[78:79], v[50:51] op_sel:[1,0,0]
	s_load_dwordx2 s[40:41], s[30:31], 0x8
	s_load_dwordx2 s[42:43], s[30:31], 0x108
	s_load_dwordx2 s[44:45], s[30:31], 0x208
	s_load_dwordx2 s[46:47], s[30:31], 0x308
	s_load_dwordx2 s[48:49], s[30:31], 0x408
	s_load_dwordx2 s[50:51], s[30:31], 0x508
	s_load_dwordx2 s[52:53], s[30:31], 0x608
	s_load_dwordx2 s[54:55], s[30:31], 0x708
	s_load_dwordx2 s[56:57], s[30:31], 0x808
	s_load_dwordx2 s[58:59], s[30:31], 0x908
	s_load_dwordx2 s[60:61], s[32:33], 0x8
	s_load_dwordx16 s[64:79], s[34:35], 0x40
	s_waitcnt lgkmcnt(0)
	v_mov_b32_e32 v42, s60
	v_mov_b32_e32 v43, s61
	v_pk_fma_f32 v[42:43], v[32:33], s[40:41], v[42:43] op_sel_hi:[0,1,1]
	v_pk_fma_f32 v[42:43], v[32:33], s[42:43], v[42:43] op_sel:[1,0,0]
	v_pk_fma_f32 v[42:43], v[34:35], s[44:45], v[42:43] op_sel_hi:[0,1,1]
	v_pk_fma_f32 v[42:43], v[34:35], s[46:47], v[42:43] op_sel:[1,0,0]
	v_pk_fma_f32 v[42:43], v[36:37], s[48:49], v[42:43] op_sel_hi:[0,1,1]
	v_pk_fma_f32 v[42:43], v[36:37], s[50:51], v[42:43] op_sel:[1,0,0]
	v_pk_fma_f32 v[42:43], v[38:39], s[52:53], v[42:43] op_sel_hi:[0,1,1]
	v_pk_fma_f32 v[42:43], v[38:39], s[54:55], v[42:43] op_sel:[1,0,0]
	v_pk_fma_f32 v[42:43], v[40:41], s[56:57], v[42:43] op_sel_hi:[0,1,1]
	v_pk_fma_f32 v[42:43], v[40:41], s[58:59], v[42:43] op_sel:[1,0,0]
	v_max_f32_e32 v42, 0, v42
	v_max_f32_e32 v43, 0, v43
	v_cvt_pk_f16_f32 v53, v42, v43
	v_pk_fma_f32 v[44:45], v[42:43], s[64:65], v[44:45] op_sel_hi:[0,1,1]
	v_pk_fma_f32 v[46:47], v[42:43], s[66:67], v[46:47] op_sel_hi:[0,1,1]
	v_pk_fma_f32 v[48:49], v[42:43], s[68:69], v[48:49] op_sel_hi:[0,1,1]
	v_pk_fma_f32 v[50:51], v[42:43], s[70:71], v[50:51] op_sel_hi:[0,1,1]
	v_pk_fma_f32 v[44:45], v[42:43], s[72:73], v[44:45] op_sel:[1,0,0]
	v_pk_fma_f32 v[46:47], v[42:43], s[74:75], v[46:47] op_sel:[1,0,0]
	v_pk_fma_f32 v[48:49], v[42:43], s[76:77], v[48:49] op_sel:[1,0,0]
	v_pk_fma_f32 v[50:51], v[42:43], s[78:79], v[50:51] op_sel:[1,0,0]
	s_load_dwordx2 s[40:41], s[30:31], 0x10
	s_load_dwordx2 s[42:43], s[30:31], 0x110
	s_load_dwordx2 s[44:45], s[30:31], 0x210
	s_load_dwordx2 s[46:47], s[30:31], 0x310
	s_load_dwordx2 s[48:49], s[30:31], 0x410
	s_load_dwordx2 s[50:51], s[30:31], 0x510
	s_load_dwordx2 s[52:53], s[30:31], 0x610
	s_load_dwordx2 s[54:55], s[30:31], 0x710
	s_load_dwordx2 s[56:57], s[30:31], 0x810
	s_load_dwordx2 s[58:59], s[30:31], 0x910
	s_load_dwordx2 s[60:61], s[32:33], 0x10
	s_load_dwordx16 s[64:79], s[34:35], 0x80
	s_waitcnt lgkmcnt(0)
	v_mov_b32_e32 v42, s60
	v_mov_b32_e32 v43, s61
	v_pk_fma_f32 v[42:43], v[32:33], s[40:41], v[42:43] op_sel_hi:[0,1,1]
	v_pk_fma_f32 v[42:43], v[32:33], s[42:43], v[42:43] op_sel:[1,0,0]
	v_pk_fma_f32 v[42:43], v[34:35], s[44:45], v[42:43] op_sel_hi:[0,1,1]
	v_pk_fma_f32 v[42:43], v[34:35], s[46:47], v[42:43] op_sel:[1,0,0]
	v_pk_fma_f32 v[42:43], v[36:37], s[48:49], v[42:43] op_sel_hi:[0,1,1]
	v_pk_fma_f32 v[42:43], v[36:37], s[50:51], v[42:43] op_sel:[1,0,0]
	v_pk_fma_f32 v[42:43], v[38:39], s[52:53], v[42:43] op_sel_hi:[0,1,1]
	v_pk_fma_f32 v[42:43], v[38:39], s[54:55], v[42:43] op_sel:[1,0,0]
	v_pk_fma_f32 v[42:43], v[40:41], s[56:57], v[42:43] op_sel_hi:[0,1,1]
	v_pk_fma_f32 v[42:43], v[40:41], s[58:59], v[42:43] op_sel:[1,0,0]
	v_max_f32_e32 v42, 0, v42
	v_max_f32_e32 v43, 0, v43
	v_cvt_pk_f16_f32 v54, v42, v43
	v_pk_fma_f32 v[44:45], v[42:43], s[64:65], v[44:45] op_sel_hi:[0,1,1]
	v_pk_fma_f32 v[46:47], v[42:43], s[66:67], v[46:47] op_sel_hi:[0,1,1]
	v_pk_fma_f32 v[48:49], v[42:43], s[68:69], v[48:49] op_sel_hi:[0,1,1]
	v_pk_fma_f32 v[50:51], v[42:43], s[70:71], v[50:51] op_sel_hi:[0,1,1]
	v_pk_fma_f32 v[44:45], v[42:43], s[72:73], v[44:45] op_sel:[1,0,0]
	v_pk_fma_f32 v[46:47], v[42:43], s[74:75], v[46:47] op_sel:[1,0,0]
	v_pk_fma_f32 v[48:49], v[42:43], s[76:77], v[48:49] op_sel:[1,0,0]
	v_pk_fma_f32 v[50:51], v[42:43], s[78:79], v[50:51] op_sel:[1,0,0]
	s_load_dwordx2 s[40:41], s[30:31], 0x18
	s_load_dwordx2 s[42:43], s[30:31], 0x118
	s_load_dwordx2 s[44:45], s[30:31], 0x218
	s_load_dwordx2 s[46:47], s[30:31], 0x318
	s_load_dwordx2 s[48:49], s[30:31], 0x418
	s_load_dwordx2 s[50:51], s[30:31], 0x518
	s_load_dwordx2 s[52:53], s[30:31], 0x618
	s_load_dwordx2 s[54:55], s[30:31], 0x718
	s_load_dwordx2 s[56:57], s[30:31], 0x818
	s_load_dwordx2 s[58:59], s[30:31], 0x918
	s_load_dwordx2 s[60:61], s[32:33], 0x18
	s_load_dwordx16 s[64:79], s[34:35], 0xc0
	s_waitcnt lgkmcnt(0)
	v_mov_b32_e32 v42, s60
	v_mov_b32_e32 v43, s61
	v_pk_fma_f32 v[42:43], v[32:33], s[40:41], v[42:43] op_sel_hi:[0,1,1]
	v_pk_fma_f32 v[42:43], v[32:33], s[42:43], v[42:43] op_sel:[1,0,0]
	v_pk_fma_f32 v[42:43], v[34:35], s[44:45], v[42:43] op_sel_hi:[0,1,1]
	v_pk_fma_f32 v[42:43], v[34:35], s[46:47], v[42:43] op_sel:[1,0,0]
	v_pk_fma_f32 v[42:43], v[36:37], s[48:49], v[42:43] op_sel_hi:[0,1,1]
	v_pk_fma_f32 v[42:43], v[36:37], s[50:51], v[42:43] op_sel:[1,0,0]
	v_pk_fma_f32 v[42:43], v[38:39], s[52:53], v[42:43] op_sel_hi:[0,1,1]
	v_pk_fma_f32 v[42:43], v[38:39], s[54:55], v[42:43] op_sel:[1,0,0]
	v_pk_fma_f32 v[42:43], v[40:41], s[56:57], v[42:43] op_sel_hi:[0,1,1]
	v_pk_fma_f32 v[42:43], v[40:41], s[58:59], v[42:43] op_sel:[1,0,0]
	v_max_f32_e32 v42, 0, v42
	v_max_f32_e32 v43, 0, v43
	v_cvt_pk_f16_f32 v55, v42, v43
	v_pk_fma_f32 v[44:45], v[42:43], s[64:65], v[44:45] op_sel_hi:[0,1,1]
	v_pk_fma_f32 v[46:47], v[42:43], s[66:67], v[46:47] op_sel_hi:[0,1,1]
	v_pk_fma_f32 v[48:49], v[42:43], s[68:69], v[48:49] op_sel_hi:[0,1,1]
	v_pk_fma_f32 v[50:51], v[42:43], s[70:71], v[50:51] op_sel_hi:[0,1,1]
	v_pk_fma_f32 v[44:45], v[42:43], s[72:73], v[44:45] op_sel:[1,0,0]
	v_pk_fma_f32 v[46:47], v[42:43], s[74:75], v[46:47] op_sel:[1,0,0]
	v_pk_fma_f32 v[48:49], v[42:43], s[76:77], v[48:49] op_sel:[1,0,0]
	v_pk_fma_f32 v[50:51], v[42:43], s[78:79], v[50:51] op_sel:[1,0,0]
	global_store_dwordx4 v60, v[52:55], s[36:37] offset:0
	s_load_dwordx2 s[40:41], s[30:31], 0x20
	s_load_dwordx2 s[42:43], s[30:31], 0x120
	s_load_dwordx2 s[44:45], s[30:31], 0x220
	s_load_dwordx2 s[46:47], s[30:31], 0x320
	s_load_dwordx2 s[48:49], s[30:31], 0x420
	s_load_dwordx2 s[50:51], s[30:31], 0x520
	s_load_dwordx2 s[52:53], s[30:31], 0x620
	s_load_dwordx2 s[54:55], s[30:31], 0x720
	s_load_dwordx2 s[56:57], s[30:31], 0x820
	s_load_dwordx2 s[58:59], s[30:31], 0x920
	s_load_dwordx2 s[60:61], s[32:33], 0x20
	s_load_dwordx16 s[64:79], s[34:35], 0x100
	s_waitcnt lgkmcnt(0)
	v_mov_b32_e32 v42, s60
	v_mov_b32_e32 v43, s61
	v_pk_fma_f32 v[42:43], v[32:33], s[40:41], v[42:43] op_sel_hi:[0,1,1]
	v_pk_fma_f32 v[42:43], v[32:33], s[42:43], v[42:43] op_sel:[1,0,0]
	v_pk_fma_f32 v[42:43], v[34:35], s[44:45], v[42:43] op_sel_hi:[0,1,1]
	v_pk_fma_f32 v[42:43], v[34:35], s[46:47], v[42:43] op_sel:[1,0,0]
	v_pk_fma_f32 v[42:43], v[36:37], s[48:49], v[42:43] op_sel_hi:[0,1,1]
	v_pk_fma_f32 v[42:43], v[36:37], s[50:51], v[42:43] op_sel:[1,0,0]
	v_pk_fma_f32 v[42:43], v[38:39], s[52:53], v[42:43] op_sel_hi:[0,1,1]
	v_pk_fma_f32 v[42:43], v[38:39], s[54:55], v[42:43] op_sel:[1,0,0]
	v_pk_fma_f32 v[42:43], v[40:41], s[56:57], v[42:43] op_sel_hi:[0,1,1]
	v_pk_fma_f32 v[42:43], v[40:41], s[58:59], v[42:43] op_sel:[1,0,0]
	v_max_f32_e32 v42, 0, v42
	v_max_f32_e32 v43, 0, v43
	v_cvt_pk_f16_f32 v52, v42, v43
	v_pk_fma_f32 v[44:45], v[42:43], s[64:65], v[44:45] op_sel_hi:[0,1,1]
	v_pk_fma_f32 v[46:47], v[42:43], s[66:67], v[46:47] op_sel_hi:[0,1,1]
	v_pk_fma_f32 v[48:49], v[42:43], s[68:69], v[48:49] op_sel_hi:[0,1,1]
	v_pk_fma_f32 v[50:51], v[42:43], s[70:71], v[50:51] op_sel_hi:[0,1,1]
	v_pk_fma_f32 v[44:45], v[42:43], s[72:73], v[44:45] op_sel:[1,0,0]
	v_pk_fma_f32 v[46:47], v[42:43], s[74:75], v[46:47] op_sel:[1,0,0]
	v_pk_fma_f32 v[48:49], v[42:43], s[76:77], v[48:49] op_sel:[1,0,0]
	v_pk_fma_f32 v[50:51], v[42:43], s[78:79], v[50:51] op_sel:[1,0,0]
	s_load_dwordx2 s[40:41], s[30:31], 0x28
	s_load_dwordx2 s[42:43], s[30:31], 0x128
	s_load_dwordx2 s[44:45], s[30:31], 0x228
	s_load_dwordx2 s[46:47], s[30:31], 0x328
	s_load_dwordx2 s[48:49], s[30:31], 0x428
	s_load_dwordx2 s[50:51], s[30:31], 0x528
	s_load_dwordx2 s[52:53], s[30:31], 0x628
	s_load_dwordx2 s[54:55], s[30:31], 0x728
	s_load_dwordx2 s[56:57], s[30:31], 0x828
	s_load_dwordx2 s[58:59], s[30:31], 0x928
	s_load_dwordx2 s[60:61], s[32:33], 0x28
	s_load_dwordx16 s[64:79], s[34:35], 0x140
	s_waitcnt lgkmcnt(0)
	v_mov_b32_e32 v42, s60
	v_mov_b32_e32 v43, s61
	v_pk_fma_f32 v[42:43], v[32:33], s[40:41], v[42:43] op_sel_hi:[0,1,1]
	v_pk_fma_f32 v[42:43], v[32:33], s[42:43], v[42:43] op_sel:[1,0,0]
	v_pk_fma_f32 v[42:43], v[34:35], s[44:45], v[42:43] op_sel_hi:[0,1,1]
	v_pk_fma_f32 v[42:43], v[34:35], s[46:47], v[42:43] op_sel:[1,0,0]
	v_pk_fma_f32 v[42:43], v[36:37], s[48:49], v[42:43] op_sel_hi:[0,1,1]
	v_pk_fma_f32 v[42:43], v[36:37], s[50:51], v[42:43] op_sel:[1,0,0]
	v_pk_fma_f32 v[42:43], v[38:39], s[52:53], v[42:43] op_sel_hi:[0,1,1]
	v_pk_fma_f32 v[42:43], v[38:39], s[54:55], v[42:43] op_sel:[1,0,0]
	v_pk_fma_f32 v[42:43], v[40:41], s[56:57], v[42:43] op_sel_hi:[0,1,1]
	v_pk_fma_f32 v[42:43], v[40:41], s[58:59], v[42:43] op_sel:[1,0,0]
	v_max_f32_e32 v42, 0, v42
	v_max_f32_e32 v43, 0, v43
	v_cvt_pk_f16_f32 v53, v42, v43
	v_pk_fma_f32 v[44:45], v[42:43], s[64:65], v[44:45] op_sel_hi:[0,1,1]
	v_pk_fma_f32 v[46:47], v[42:43], s[66:67], v[46:47] op_sel_hi:[0,1,1]
	v_pk_fma_f32 v[48:49], v[42:43], s[68:69], v[48:49] op_sel_hi:[0,1,1]
	v_pk_fma_f32 v[50:51], v[42:43], s[70:71], v[50:51] op_sel_hi:[0,1,1]
	v_pk_fma_f32 v[44:45], v[42:43], s[72:73], v[44:45] op_sel:[1,0,0]
	v_pk_fma_f32 v[46:47], v[42:43], s[74:75], v[46:47] op_sel:[1,0,0]
	v_pk_fma_f32 v[48:49], v[42:43], s[76:77], v[48:49] op_sel:[1,0,0]
	v_pk_fma_f32 v[50:51], v[42:43], s[78:79], v[50:51] op_sel:[1,0,0]
	s_load_dwordx2 s[40:41], s[30:31], 0x30
	s_load_dwordx2 s[42:43], s[30:31], 0x130
	s_load_dwordx2 s[44:45], s[30:31], 0x230
	s_load_dwordx2 s[46:47], s[30:31], 0x330
	s_load_dwordx2 s[48:49], s[30:31], 0x430
	s_load_dwordx2 s[50:51], s[30:31], 0x530
	s_load_dwordx2 s[52:53], s[30:31], 0x630
	s_load_dwordx2 s[54:55], s[30:31], 0x730
	s_load_dwordx2 s[56:57], s[30:31], 0x830
	s_load_dwordx2 s[58:59], s[30:31], 0x930
	s_load_dwordx2 s[60:61], s[32:33], 0x30
	s_load_dwordx16 s[64:79], s[34:35], 0x180
	s_waitcnt lgkmcnt(0)
	v_mov_b32_e32 v42, s60
	v_mov_b32_e32 v43, s61
	v_pk_fma_f32 v[42:43], v[32:33], s[40:41], v[42:43] op_sel_hi:[0,1,1]
	v_pk_fma_f32 v[42:43], v[32:33], s[42:43], v[42:43] op_sel:[1,0,0]
	v_pk_fma_f32 v[42:43], v[34:35], s[44:45], v[42:43] op_sel_hi:[0,1,1]
	v_pk_fma_f32 v[42:43], v[34:35], s[46:47], v[42:43] op_sel:[1,0,0]
	v_pk_fma_f32 v[42:43], v[36:37], s[48:49], v[42:43] op_sel_hi:[0,1,1]
	v_pk_fma_f32 v[42:43], v[36:37], s[50:51], v[42:43] op_sel:[1,0,0]
	v_pk_fma_f32 v[42:43], v[38:39], s[52:53], v[42:43] op_sel_hi:[0,1,1]
	v_pk_fma_f32 v[42:43], v[38:39], s[54:55], v[42:43] op_sel:[1,0,0]
	v_pk_fma_f32 v[42:43], v[40:41], s[56:57], v[42:43] op_sel_hi:[0,1,1]
	v_pk_fma_f32 v[42:43], v[40:41], s[58:59], v[42:43] op_sel:[1,0,0]
	v_max_f32_e32 v42, 0, v42
	v_max_f32_e32 v43, 0, v43
	v_cvt_pk_f16_f32 v54, v42, v43
	v_pk_fma_f32 v[44:45], v[42:43], s[64:65], v[44:45] op_sel_hi:[0,1,1]
	v_pk_fma_f32 v[46:47], v[42:43], s[66:67], v[46:47] op_sel_hi:[0,1,1]
	v_pk_fma_f32 v[48:49], v[42:43], s[68:69], v[48:49] op_sel_hi:[0,1,1]
	v_pk_fma_f32 v[50:51], v[42:43], s[70:71], v[50:51] op_sel_hi:[0,1,1]
	v_pk_fma_f32 v[44:45], v[42:43], s[72:73], v[44:45] op_sel:[1,0,0]
	v_pk_fma_f32 v[46:47], v[42:43], s[74:75], v[46:47] op_sel:[1,0,0]
	v_pk_fma_f32 v[48:49], v[42:43], s[76:77], v[48:49] op_sel:[1,0,0]
	v_pk_fma_f32 v[50:51], v[42:43], s[78:79], v[50:51] op_sel:[1,0,0]
	s_load_dwordx2 s[40:41], s[30:31], 0x38
	s_load_dwordx2 s[42:43], s[30:31], 0x138
	s_load_dwordx2 s[44:45], s[30:31], 0x238
	s_load_dwordx2 s[46:47], s[30:31], 0x338
	s_load_dwordx2 s[48:49], s[30:31], 0x438
	s_load_dwordx2 s[50:51], s[30:31], 0x538
	s_load_dwordx2 s[52:53], s[30:31], 0x638
	s_load_dwordx2 s[54:55], s[30:31], 0x738
	s_load_dwordx2 s[56:57], s[30:31], 0x838
	s_load_dwordx2 s[58:59], s[30:31], 0x938
	s_load_dwordx2 s[60:61], s[32:33], 0x38
	s_load_dwordx16 s[64:79], s[34:35], 0x1c0
	s_waitcnt lgkmcnt(0)
	v_mov_b32_e32 v42, s60
	v_mov_b32_e32 v43, s61
	v_pk_fma_f32 v[42:43], v[32:33], s[40:41], v[42:43] op_sel_hi:[0,1,1]
	v_pk_fma_f32 v[42:43], v[32:33], s[42:43], v[42:43] op_sel:[1,0,0]
	v_pk_fma_f32 v[42:43], v[34:35], s[44:45], v[42:43] op_sel_hi:[0,1,1]
	v_pk_fma_f32 v[42:43], v[34:35], s[46:47], v[42:43] op_sel:[1,0,0]
	v_pk_fma_f32 v[42:43], v[36:37], s[48:49], v[42:43] op_sel_hi:[0,1,1]
	v_pk_fma_f32 v[42:43], v[36:37], s[50:51], v[42:43] op_sel:[1,0,0]
	v_pk_fma_f32 v[42:43], v[38:39], s[52:53], v[42:43] op_sel_hi:[0,1,1]
	v_pk_fma_f32 v[42:43], v[38:39], s[54:55], v[42:43] op_sel:[1,0,0]
	v_pk_fma_f32 v[42:43], v[40:41], s[56:57], v[42:43] op_sel_hi:[0,1,1]
	v_pk_fma_f32 v[42:43], v[40:41], s[58:59], v[42:43] op_sel:[1,0,0]
	v_max_f32_e32 v42, 0, v42
	v_max_f32_e32 v43, 0, v43
	v_cvt_pk_f16_f32 v55, v42, v43
	v_pk_fma_f32 v[44:45], v[42:43], s[64:65], v[44:45] op_sel_hi:[0,1,1]
	v_pk_fma_f32 v[46:47], v[42:43], s[66:67], v[46:47] op_sel_hi:[0,1,1]
	v_pk_fma_f32 v[48:49], v[42:43], s[68:69], v[48:49] op_sel_hi:[0,1,1]
	v_pk_fma_f32 v[50:51], v[42:43], s[70:71], v[50:51] op_sel_hi:[0,1,1]
	v_pk_fma_f32 v[44:45], v[42:43], s[72:73], v[44:45] op_sel:[1,0,0]
	v_pk_fma_f32 v[46:47], v[42:43], s[74:75], v[46:47] op_sel:[1,0,0]
	v_pk_fma_f32 v[48:49], v[42:43], s[76:77], v[48:49] op_sel:[1,0,0]
	v_pk_fma_f32 v[50:51], v[42:43], s[78:79], v[50:51] op_sel:[1,0,0]
	global_store_dwordx4 v60, v[52:55], s[36:37] offset:16
	ds_write_b128 v61, v[44:47]
	ds_write_b128 v61, v[48:51] offset:16
	s_or_b64 exec, exec, s[38:39]
	s_waitcnt lgkmcnt(0)
	s_waitcnt vmcnt(2)
	s_branch .Lc7_cnt

.LBB2_74:
	s_mov_b64 exec, -1
	s_load_dwordx4 s[28:31], s[0:1], 0x48
	s_lshl_b32 s62, s27, 8
	v_add_u32_e32 v1, s62, v0
	v_cmp_gt_u32_e32 vcc, 0x100, v0
	s_mov_b32 s63, 0x186a0
	v_cmp_gt_i32_e64 s[38:39], s63, v1
	s_and_b64 vcc, vcc, s[38:39]
	s_and_saveexec_b64 s[38:39], vcc
	s_cbranch_execz .Ln0b_fin_done
	v_lshlrev_b32_e32 v2, 3, v1
	v_lshlrev_b32_e32 v3, 4, v1
	v_lshlrev_b32_e32 v4, 7, v0
	v_add_u32_e32 v4, 0x1740, v4
	v_and_b32_e32 v5, 3, v0
	v_lshlrev_b32_e32 v5, 5, v5
	v_xor_b32_e32 v6, 32, v5
	v_xor_b32_e32 v7, 64, v5
	v_xor_b32_e32 v8, 0x60, v5
	v_add_u32_e32 v5, v4, v5
	v_add_u32_e32 v6, v4, v6
	v_add_u32_e32 v7, v4, v7
	v_add_u32_e32 v8, v4, v8
	ds_read_b128 v[32:35], v5
	ds_read_b128 v[36:39], v5 offset:16
	ds_read_b128 v[40:43], v6
	ds_read_b128 v[44:47], v6 offset:16
	ds_read_b128 v[48:51], v7
	ds_read_b128 v[52:55], v7 offset:16
	ds_read_b128 v[56:59], v8
	ds_read_b128 v[60:63], v8 offset:16
	s_waitcnt lgkmcnt(0)
	v_pk_add_f32 v[32:33], v[32:33], v[40:41]
	v_pk_add_f32 v[48:49], v[48:49], v[56:57]
	v_pk_add_f32 v[34:35], v[34:35], v[42:43]
	v_pk_add_f32 v[50:51], v[50:51], v[58:59]
	v_pk_add_f32 v[36:37], v[36:37], v[44:45]
	v_pk_add_f32 v[52:53], v[52:53], v[60:61]
	v_pk_add_f32 v[38:39], v[38:39], v[46:47]
	v_pk_add_f32 v[54:55], v[54:55], v[62:63]
	v_pk_add_f32 v[32:33], v[32:33], v[48:49]
	v_pk_add_f32 v[34:35], v[34:35], v[50:51]
	v_pk_add_f32 v[36:37], v[36:37], v[52:53]
	v_pk_add_f32 v[38:39], v[38:39], v[54:55]
	v_cvt_pk_f16_f32 v40, v32, v33
	v_cvt_pk_f16_f32 v41, v34, v35
	global_store_dwordx2 v2, v[40:41], s[28:29]
	global_store_dwordx4 v3, v[36:39], s[30:31]
